# v22 plus prep: lane^32 max via permlane32_swap instead of ds_bpermute, max3 chain split into two independent chains
# baseline (speedup 1.0000x reference)
.LBB0_11:
	s_cmp_lg_u32 s20, 0
	s_cselect_b64 s[34:35], -1, 0
	v_cndmask_b32_e64 v140, v128, v183, s[34:35]
	v_cmp_gt_i32_e32 vcc, s24, v140
	s_or_b64 s[16:17], s[16:17], exec
	s_and_saveexec_b64 s[18:19], vcc
	s_cbranch_execz .LBB0_10
	v_or_b32_e32 v64, s20, v129
	v_mad_u32_u24 v141, v64, s22, v131
	ds_read_b128 v[142:145], v141
	ds_read_b128 v[146:149], v141 offset:32
	ds_read_b128 v[64:67], v136
	ds_read_b128 v[150:153], v136 offset:32
	ds_read_b128 v[68:71], v136 offset:4352
	ds_read_b128 v[154:157], v136 offset:4384
	ds_read_b128 v[72:75], v136 offset:8704
	ds_read_b128 v[158:161], v136 offset:8736
	ds_read_b128 v[162:165], v136 offset:13056
	ds_read_b128 v[166:169], v136 offset:13088
	s_waitcnt lgkmcnt(7)
	v_mfma_f32_32x32x16_bf16 v[112:127], v[64:67], v[142:145], v[0:15]
	s_waitcnt lgkmcnt(5)
	v_mfma_f32_32x32x16_bf16 v[96:111], v[68:71], v[142:145], v[16:31]
	s_waitcnt lgkmcnt(3)
	v_mfma_f32_32x32x16_bf16 v[80:95], v[72:75], v[142:145], v[32:47]
	s_waitcnt lgkmcnt(1)
	v_mfma_f32_32x32x16_bf16 v[64:79], v[162:165], v[142:145], v[48:63]
	ds_read_b128 v[142:145], v141 offset:64
	ds_read_b128 v[162:165], v136 offset:64
	ds_read_b128 v[170:173], v136 offset:4416
	ds_read_b128 v[174:177], v136 offset:8768
	ds_read_b128 v[178:181], v136 offset:13120
	v_mfma_f32_32x32x16_bf16 v[96:111], v[154:157], v[146:149], v[96:111]
	s_waitcnt lgkmcnt(5)
	v_mfma_f32_32x32x16_bf16 v[64:79], v[166:169], v[146:149], v[64:79]
	v_mfma_f32_32x32x16_bf16 v[112:127], v[150:153], v[146:149], v[112:127]
	v_mfma_f32_32x32x16_bf16 v[80:95], v[158:161], v[146:149], v[80:95]
	ds_read_b128 v[146:149], v141 offset:96
	ds_read_b128 v[150:153], v136 offset:96
	ds_read_b128 v[154:157], v136 offset:4448
	ds_read_b128 v[158:161], v136 offset:8800
	ds_read_b128 v[166:169], v136 offset:13152
	s_waitcnt lgkmcnt(7)
	v_mfma_f32_32x32x16_bf16 v[96:111], v[170:173], v[142:145], v[96:111]
	s_waitcnt lgkmcnt(5)
	v_mfma_f32_32x32x16_bf16 v[64:79], v[178:181], v[142:145], v[64:79]
	v_mfma_f32_32x32x16_bf16 v[112:127], v[162:165], v[142:145], v[112:127]
	v_mfma_f32_32x32x16_bf16 v[80:95], v[174:177], v[142:145], v[80:95]
	ds_read_b128 v[142:145], v141 offset:128
	ds_read_b128 v[162:165], v136 offset:128
	ds_read_b128 v[170:173], v136 offset:4480
	ds_read_b128 v[174:177], v136 offset:8832
	ds_read_b128 v[178:181], v136 offset:13184
	s_waitcnt lgkmcnt(7)
	v_mfma_f32_32x32x16_bf16 v[96:111], v[154:157], v[146:149], v[96:111]
	s_waitcnt lgkmcnt(5)
	v_mfma_f32_32x32x16_bf16 v[64:79], v[166:169], v[146:149], v[64:79]
	v_mfma_f32_32x32x16_bf16 v[112:127], v[150:153], v[146:149], v[112:127]
	v_mfma_f32_32x32x16_bf16 v[80:95], v[158:161], v[146:149], v[80:95]
	ds_read_b128 v[146:149], v141 offset:160
	ds_read_b128 v[150:153], v136 offset:160
	ds_read_b128 v[154:157], v136 offset:4512
	ds_read_b128 v[158:161], v136 offset:8864
	ds_read_b128 v[166:169], v136 offset:13216
	s_waitcnt lgkmcnt(7)
	v_mfma_f32_32x32x16_bf16 v[96:111], v[170:173], v[142:145], v[96:111]
	s_waitcnt lgkmcnt(5)
	v_mfma_f32_32x32x16_bf16 v[64:79], v[178:181], v[142:145], v[64:79]
	v_mfma_f32_32x32x16_bf16 v[112:127], v[162:165], v[142:145], v[112:127]
	v_mfma_f32_32x32x16_bf16 v[80:95], v[174:177], v[142:145], v[80:95]
	ds_read_b128 v[142:145], v141 offset:192
	ds_read_b128 v[162:165], v136 offset:192
	ds_read_b128 v[170:173], v136 offset:4544
	ds_read_b128 v[174:177], v136 offset:8896
	ds_read_b128 v[178:181], v136 offset:13248
	s_waitcnt lgkmcnt(7)
	v_mfma_f32_32x32x16_bf16 v[96:111], v[154:157], v[146:149], v[96:111]
	s_waitcnt lgkmcnt(5)
	v_mfma_f32_32x32x16_bf16 v[64:79], v[166:169], v[146:149], v[64:79]
	v_mfma_f32_32x32x16_bf16 v[112:127], v[150:153], v[146:149], v[112:127]
	v_mfma_f32_32x32x16_bf16 v[80:95], v[158:161], v[146:149], v[80:95]
	ds_read_b128 v[146:149], v141 offset:224
	ds_read_b128 v[150:153], v136 offset:224
	ds_read_b128 v[154:157], v136 offset:4576
	ds_read_b128 v[158:161], v136 offset:8928
	ds_read_b128 v[166:169], v136 offset:13280
	s_waitcnt lgkmcnt(7)
	v_mfma_f32_32x32x16_bf16 v[96:111], v[170:173], v[142:145], v[96:111]
	s_waitcnt lgkmcnt(5)
	v_mfma_f32_32x32x16_bf16 v[64:79], v[178:181], v[142:145], v[64:79]
	v_mfma_f32_32x32x16_bf16 v[112:127], v[162:165], v[142:145], v[112:127]
	v_mfma_f32_32x32x16_bf16 v[80:95], v[174:177], v[142:145], v[80:95]
	s_waitcnt lgkmcnt(2)
	v_mfma_f32_32x32x16_bf16 v[96:111], v[154:157], v[146:149], v[96:111]
	s_waitcnt lgkmcnt(0)
	v_mfma_f32_32x32x16_bf16 v[64:79], v[166:169], v[146:149], v[64:79]
	v_mfma_f32_32x32x16_bf16 v[112:127], v[150:153], v[146:149], v[112:127]
	v_mfma_f32_32x32x16_bf16 v[80:95], v[158:161], v[146:149], v[80:95]
	s_nop 10
	v_max3_f32 v141, |v112|, s25, |v113|
	v_max3_f32 v144, |v114|, s25, |v115|
	v_max3_f32 v141, v141, |v116|, |v117|
	v_max3_f32 v144, v144, |v118|, |v119|
	v_max3_f32 v141, v141, |v120|, |v121|
	v_max3_f32 v144, v144, |v122|, |v123|
	v_max3_f32 v141, v141, |v124|, |v125|
	v_max3_f32 v144, v144, |v126|, |v127|
	v_max3_f32 v141, v141, |v96|, |v97|
	v_max3_f32 v144, v144, |v98|, |v99|
	v_max3_f32 v141, v141, |v100|, |v101|
	v_max3_f32 v144, v144, |v102|, |v103|
	v_max3_f32 v141, v141, |v104|, |v105|
	v_max3_f32 v144, v144, |v106|, |v107|
	v_max3_f32 v141, v141, |v108|, |v109|
	v_max3_f32 v144, v144, |v110|, |v111|
	v_max3_f32 v141, v141, |v80|, |v81|
	v_max3_f32 v144, v144, |v82|, |v83|
	v_max3_f32 v141, v141, |v84|, |v85|
	v_max3_f32 v144, v144, |v86|, |v87|
	v_max3_f32 v141, v141, |v88|, |v89|
	v_max3_f32 v144, v144, |v90|, |v91|
	v_max3_f32 v141, v141, |v92|, |v93|
	v_max3_f32 v144, v144, |v94|, |v95|
	v_max3_f32 v141, v141, |v64|, |v65|
	v_max3_f32 v144, v144, |v66|, |v67|
	v_max3_f32 v141, v141, |v68|, |v69|
	v_max3_f32 v144, v144, |v70|, |v71|
	v_max3_f32 v141, v141, |v72|, |v73|
	v_max3_f32 v144, v144, |v74|, |v75|
	v_max3_f32 v141, v141, |v76|, |v77|
	v_max3_f32 v144, v144, |v78|, |v79|
	v_max_f32_e32 v141, v141, v144
	v_mov_b32_e32 v142, v141
	v_mov_b32_e32 v143, v141
	s_nop 1
	v_permlane32_swap_b32_e32 v142, v143
	s_nop 0
	v_max_f32_e32 v141, v142, v143
	v_rcp_f32_e32 v142, v141
	s_mov_b32 s30, 0x0c0c0400
	s_mov_b32 s31, 0x04000c0c
	v_mul_f32_e32 v142, 0x42fe0000, v142
	v_fmaak_f32 v216, v112, v142, 0x4b000080
	v_fmaak_f32 v217, v113, v142, 0x4b000080
	v_fmaak_f32 v218, v114, v142, 0x4b000080
	v_fmaak_f32 v219, v115, v142, 0x4b000080
	v_perm_b32 v216, v217, v216, s30
	v_perm_b32 v218, v219, v218, s31
	v_or_b32_e32 v200, v216, v218
	v_fmaak_f32 v220, v96, v142, 0x4b000080
	v_fmaak_f32 v221, v97, v142, 0x4b000080
	v_fmaak_f32 v222, v98, v142, 0x4b000080
	v_fmaak_f32 v223, v99, v142, 0x4b000080
	v_perm_b32 v220, v221, v220, s30
	v_perm_b32 v222, v223, v222, s31
	v_or_b32_e32 v201, v220, v222
	v_fmaak_f32 v216, v80, v142, 0x4b000080
	v_fmaak_f32 v217, v81, v142, 0x4b000080
	v_fmaak_f32 v218, v82, v142, 0x4b000080
	v_fmaak_f32 v219, v83, v142, 0x4b000080
	v_perm_b32 v216, v217, v216, s30
	v_perm_b32 v218, v219, v218, s31
	v_or_b32_e32 v202, v216, v218
	v_fmaak_f32 v220, v64, v142, 0x4b000080
	v_fmaak_f32 v221, v65, v142, 0x4b000080
	v_fmaak_f32 v222, v66, v142, 0x4b000080
	v_fmaak_f32 v223, v67, v142, 0x4b000080
	v_perm_b32 v220, v221, v220, s30
	v_perm_b32 v222, v223, v222, s31
	v_or_b32_e32 v203, v220, v222
	v_fmaak_f32 v216, v116, v142, 0x4b000080
	v_fmaak_f32 v217, v117, v142, 0x4b000080
	v_fmaak_f32 v218, v118, v142, 0x4b000080
	v_fmaak_f32 v219, v119, v142, 0x4b000080
	v_perm_b32 v216, v217, v216, s30
	v_perm_b32 v218, v219, v218, s31
	v_or_b32_e32 v204, v216, v218
	v_fmaak_f32 v220, v100, v142, 0x4b000080
	v_fmaak_f32 v221, v101, v142, 0x4b000080
	v_fmaak_f32 v222, v102, v142, 0x4b000080
	v_fmaak_f32 v223, v103, v142, 0x4b000080
	v_perm_b32 v220, v221, v220, s30
	v_perm_b32 v222, v223, v222, s31
	v_or_b32_e32 v205, v220, v222
	v_fmaak_f32 v216, v84, v142, 0x4b000080
	v_fmaak_f32 v217, v85, v142, 0x4b000080
	v_fmaak_f32 v218, v86, v142, 0x4b000080
	v_fmaak_f32 v219, v87, v142, 0x4b000080
	v_perm_b32 v216, v217, v216, s30
	v_perm_b32 v218, v219, v218, s31
	v_or_b32_e32 v206, v216, v218
	v_fmaak_f32 v220, v68, v142, 0x4b000080
	v_fmaak_f32 v221, v69, v142, 0x4b000080
	v_fmaak_f32 v222, v70, v142, 0x4b000080
	v_fmaak_f32 v223, v71, v142, 0x4b000080
	v_perm_b32 v220, v221, v220, s30
	v_perm_b32 v222, v223, v222, s31
	v_or_b32_e32 v207, v220, v222
	v_fmaak_f32 v216, v120, v142, 0x4b000080
	v_fmaak_f32 v217, v121, v142, 0x4b000080
	v_fmaak_f32 v218, v122, v142, 0x4b000080
	v_fmaak_f32 v219, v123, v142, 0x4b000080
	v_perm_b32 v216, v217, v216, s30
	v_perm_b32 v218, v219, v218, s31
	v_or_b32_e32 v208, v216, v218
	v_fmaak_f32 v220, v104, v142, 0x4b000080
	v_fmaak_f32 v221, v105, v142, 0x4b000080
	v_fmaak_f32 v222, v106, v142, 0x4b000080
	v_fmaak_f32 v223, v107, v142, 0x4b000080
	v_perm_b32 v220, v221, v220, s30
	v_perm_b32 v222, v223, v222, s31
	v_or_b32_e32 v209, v220, v222
	v_fmaak_f32 v216, v88, v142, 0x4b000080
	v_fmaak_f32 v217, v89, v142, 0x4b000080
	v_fmaak_f32 v218, v90, v142, 0x4b000080
	v_fmaak_f32 v219, v91, v142, 0x4b000080
	v_perm_b32 v216, v217, v216, s30
	v_perm_b32 v218, v219, v218, s31
	v_or_b32_e32 v210, v216, v218
	v_fmaak_f32 v220, v72, v142, 0x4b000080
	v_fmaak_f32 v221, v73, v142, 0x4b000080
	v_fmaak_f32 v222, v74, v142, 0x4b000080
	v_fmaak_f32 v223, v75, v142, 0x4b000080
	v_perm_b32 v220, v221, v220, s30
	v_perm_b32 v222, v223, v222, s31
	v_or_b32_e32 v211, v220, v222
	v_fmaak_f32 v216, v124, v142, 0x4b000080
	v_fmaak_f32 v217, v125, v142, 0x4b000080
	v_fmaak_f32 v218, v126, v142, 0x4b000080
	v_fmaak_f32 v219, v127, v142, 0x4b000080
	v_perm_b32 v216, v217, v216, s30
	v_perm_b32 v218, v219, v218, s31
	v_or_b32_e32 v212, v216, v218
	v_fmaak_f32 v220, v108, v142, 0x4b000080
	v_fmaak_f32 v221, v109, v142, 0x4b000080
	v_fmaak_f32 v222, v110, v142, 0x4b000080
	v_fmaak_f32 v223, v111, v142, 0x4b000080
	v_perm_b32 v220, v221, v220, s30
	v_perm_b32 v222, v223, v222, s31
	v_or_b32_e32 v213, v220, v222
	v_fmaak_f32 v216, v92, v142, 0x4b000080
	v_fmaak_f32 v217, v93, v142, 0x4b000080
	v_fmaak_f32 v218, v94, v142, 0x4b000080
	v_fmaak_f32 v219, v95, v142, 0x4b000080
	v_perm_b32 v216, v217, v216, s30
	v_perm_b32 v218, v219, v218, s31
	v_or_b32_e32 v214, v216, v218
	v_fmaak_f32 v220, v76, v142, 0x4b000080
	v_fmaak_f32 v221, v77, v142, 0x4b000080
	v_fmaak_f32 v222, v78, v142, 0x4b000080
	v_fmaak_f32 v223, v79, v142, 0x4b000080
	v_perm_b32 v220, v221, v220, s30
	v_perm_b32 v222, v223, v222, s31
	v_or_b32_e32 v215, v220, v222
	s_and_saveexec_b64 s[20:21], s[2:3]
	s_cbranch_execz .LBB0_14
	ds_write_b128 v138, v[200:203]
	ds_write_b128 v138, v[204:207] offset:16
	ds_write_b128 v138, v[208:211] offset:32
	ds_write_b128 v138, v[212:215] offset:48
